# adds: P7/P10 parameter-to-LDS fill loops unrolled (8 loads in flight, one wait) on top of P6 epilogue prefetch + P8 set-up batching
# speedup vs baseline: 1.0089x; 1.0089x over previous
; __global__ void __launch_bounds__(NTHREADS, 2) fwd(Args args) {
;     ...
;         for (int i = tid; i < D; i += NTHREADS) { LG1[i] = ln1_g[i]; LB1[i] = ln1_b[i]; }
;         const int GPW = (T / 32 + G - 1) / G; int bprev = -1;
;         for (int gi = bid * GPW; gi < bid * GPW + GPW && gi < T / 32; ++gi) { const int g0 = gi * 32;
.LBB0_756:
	global_load_dword v9, v[2:3], off
	global_load_dword v10, v[4:5], off
	global_load_dword v11, v[2:3], off offset:2048
	global_load_dword v12, v[4:5], off offset:2048
	v_lshl_add_u64 v[2:3], v[2:3], 0, s[8:9]
	v_lshl_add_u64 v[4:5], v[4:5], 0, s[8:9]
	v_lshl_add_u64 v[2:3], v[2:3], 0, s[8:9]
	v_lshl_add_u64 v[4:5], v[4:5], 0, s[8:9]
	global_load_dword v13, v[2:3], off
	global_load_dword v14, v[4:5], off
	global_load_dword v15, v[2:3], off offset:2048
	global_load_dword v16, v[4:5], off offset:2048
	s_waitcnt vmcnt(0)
	ds_write2st64_b32 v7, v9, v10 offset1:32
	ds_write2st64_b32 v7, v11, v12 offset0:8 offset1:40
	ds_write2st64_b32 v7, v13, v14 offset0:16 offset1:48
	ds_write2st64_b32 v7, v15, v16 offset0:24 offset1:56
	s_or_b64 exec, exec, s[6:7]
	v_readlane_b32 s2, v246, 10
	s_mov_b32 s6, s2
	s_abs_i32 s2, s2
	v_cvt_f32_u32_e32 v2, s2
	s_sub_i32 s7, 0, s2
	v_readlane_b32 s3, v246, 11
	s_add_i32 s3, s6, 0x1ff
	v_rcp_iflag_f32_e32 v2, v2
	s_xor_b32 s6, s3, s6
	s_abs_i32 s3, s3
	s_ashr_i32 s6, s6, 31
	v_mul_f32_e32 v2, 0x4f7ffffe, v2
	v_cvt_u32_f32_e32 v2, v2
	s_nop 0
	v_readfirstlane_b32 s8, v2
	s_mul_i32 s7, s7, s8
	s_mul_hi_u32 s7, s8, s7
	s_add_i32 s8, s8, s7
	s_mul_hi_u32 s7, s3, s8
	s_mul_i32 s8, s7, s2
	s_sub_i32 s3, s3, s8
	s_add_i32 s9, s7, 1
	s_sub_i32 s8, s3, s2
	s_cmp_ge_u32 s3, s2
	s_cselect_b32 s7, s9, s7
	s_cselect_b32 s3, s8, s3
	s_add_i32 s8, s7, 1
	s_cmp_ge_u32 s3, s2
	s_cselect_b32 s2, s8, s7
	s_xor_b32 s2, s2, s6
	s_sub_i32 s3, s2, s6
	s_mul_i32 s2, s3, s94
	s_add_i32 s3, s2, s3
	s_min_i32 s3, s3, 0x200
	s_cmp_ge_i32 s2, s3
	s_cbranch_scc1 .LBB0_792
	v_and_b32_e32 v200, 31, v0
	v_readlane_b32 s6, v246, 19
	s_add_u32 s30, s88, 0x5f600000
	v_lshrrev_b32_e32 v3, 5, v220
	v_lshlrev_b32_e32 v146, 12, v200
	v_mov_b32_e32 v147, 0
	v_readlane_b32 s7, v246, 20
	s_addc_u32 s31, s89, 0
	v_lshlrev_b32_e32 v4, 3, v3
	v_lshl_add_u64 v[148:149], s[6:7], 0, v[146:147]
	v_lshl_add_u64 v[150:151], s[48:49], 0, v[146:147]
	v_lshlrev_b32_e32 v3, 9, v3
	v_lshlrev_b32_e32 v146, 2, v200
	s_add_u32 s34, s88, 0x63700000
	v_add3_u32 v5, 0, v3, v146
	v_lshl_add_u64 v[152:153], s[64:65], 0, v[146:147]
	v_lshlrev_b32_e32 v146, 8, v0
	s_addc_u32 s35, s89, 0
	v_lshlrev_b32_e32 v2, 3, v220
	v_lshl_add_u64 v[154:155], s[28:29], 0, v[146:147]
	v_mov_b32_e32 v3, v147
	v_lshlrev_b32_e32 v146, 4, v220
	s_add_u32 s36, s88, 0x85a00000
	v_readlane_b32 s39, v246, 21
	v_lshl_add_u64 v[156:157], s[14:15], 0, v[146:147]
	v_lshl_add_u64 v[164:165], s[26:27], 0, v[2:3]
	v_lshl_add_u64 v[2:3], s[88:89], 0, v[194:195]
	s_mov_b64 s[14:15], 0x108000
	s_addc_u32 s37, s89, 0
	v_lshl_add_u64 v[166:167], v[2:3], 0, s[14:15]
	s_lshl_b32 s14, s2, 7
	s_lshl_b32 s15, s39, 4
	s_add_i32 s14, s14, s15
	v_add_u32_e32 v211, s14, v220
	s_lshl_b32 s14, s39, 9
	v_lshlrev_b32_e32 v7, 2, v220
	s_add_i32 s14, s14, 0
	v_add_u32_e32 v2, s14, v7
	s_lshl_b32 s14, s39, 6
	s_add_i32 s14, s14, 0
	s_add_i32 s38, 0, 0x10000
	v_add_u32_e32 v212, 0x8000, v2
	v_add_u32_e32 v2, s14, v7
	s_lshl_b32 s40, s39, 12
	s_movk_i32 s12, 0x80
	v_mul_u32_u24_e32 v8, 28, v220
	v_lshl_add_u32 v202, v220, 5, s38
	v_add_u32_e32 v213, 0x9000, v2
	v_mbcnt_lo_u32_b32 v2, -1, 0
	s_lshl_b32 s33, s39, 2
	v_cmp_gt_u32_e64 s[6:7], 32, v220
	v_cmp_gt_u32_e64 s[8:9], 4, v220
	v_cmp_eq_u32_e64 s[10:11], 2, v220
	v_cmp_gt_u32_e64 s[12:13], s12, v0
	v_add3_u32 v201, 0, v7, v8
	v_add_u32_e32 v203, 16, v202
	v_add_u32_e32 v204, 0x800, v202
	v_add_u32_e32 v205, 0x810, v202
	v_add_u32_e32 v206, 0x1000, v202
	v_add_u32_e32 v207, 0x1010, v202
	v_add_u32_e32 v208, 0x1800, v202
	v_add_u32_e32 v209, 0x1810, v202
	v_lshl_add_u64 v[158:159], s[22:23], 0, v[146:147]
	v_lshl_add_u64 v[160:161], s[30:31], 0, v[146:147]
	v_lshl_add_u64 v[162:163], s[36:37], 0, v[146:147]
	v_add_u32_e32 v210, 0xe000, v6
	v_lshl_or_b32 v195, s39, 8, v4
	s_mov_b32 s56, -1
	s_mov_b64 s[38:39], 0x800
	s_movk_i32 s51, 0x5ff
	v_mbcnt_hi_u32_b32 v214, -1, v2
	v_mov_b32_e32 v215, 0x3727c5ac
	s_mov_b32 s52, 0xf800000
	v_mov_b32_e32 v216, 0x260
	v_add_u32_e32 v217, s40, v5
	s_mov_b32 s53, 0x3fb8aa3b
	s_mov_b32 s54, 0xc2ce8ed0
	s_mov_b32 s55, 0x42b17218
	v_mov_b32_e32 v218, 1
	v_mov_b32_e32 v219, 0xff800000
	v_mov_b32_e32 v223, 0x7f800000
	s_branch .LBB0_760

; __global__ void __launch_bounds__(NTHREADS, 2) fwd(Args args) {
;     ...
;             if (g0 / SEQ != bprev) { bprev = g0 / SEQ; const float* sh2g = MOD + (g0 / SEQ) * (6 * D) + 3 * D; for (int i = tid; i < D; i += NTHREADS) { SH2[i] = sh2g[i]; SC2[i] = sh2g[D + i]; } }
.LBB0_762:
	v_add_co_u32_e32 v6, vcc, 0xffffe000, v2
	s_nop 1
	v_addc_co_u32_e32 v7, vcc, -1, v3, vcc
	global_load_dword v8, v[6:7], off
	global_load_dword v9, v[2:3], off
	global_load_dword v10, v[6:7], off offset:2048
	global_load_dword v11, v[2:3], off offset:2048
	v_lshl_add_u64 v[6:7], v[6:7], 0, s[38:39]
	v_lshl_add_u64 v[2:3], v[2:3], 0, s[38:39]
	v_lshl_add_u64 v[6:7], v[6:7], 0, s[38:39]
	v_lshl_add_u64 v[2:3], v[2:3], 0, s[38:39]
	global_load_dword v12, v[6:7], off
	global_load_dword v13, v[2:3], off
	global_load_dword v6, v[6:7], off offset:2048
	global_load_dword v7, v[2:3], off offset:2048
	s_waitcnt vmcnt(0)
	ds_write2st64_b32 v5, v8, v9 offset1:32
	ds_write2st64_b32 v5, v10, v11 offset0:8 offset1:40
	ds_write2st64_b32 v5, v12, v13 offset0:16 offset1:48
	ds_write2st64_b32 v5, v6, v7 offset0:24 offset1:56
	s_or_b64 exec, exec, s[14:15]
	s_mov_b32 s56, s40

; __global__ void __launch_bounds__(NTHREADS, 2) fwd(Args args) {
;     ...
;         for (int i = tid; i < D; i += NTHREADS) { LG[i] = ln2_g[i]; LB[i] = ln2_b[i]; }
.LBB0_1222:
	global_load_dword v5, v[0:1], off
	global_load_dword v6, v[2:3], off
	global_load_dword v7, v[0:1], off offset:2048
	global_load_dword v8, v[2:3], off offset:2048
	v_lshl_add_u64 v[0:1], v[0:1], 0, s[10:11]
	v_lshl_add_u64 v[2:3], v[2:3], 0, s[10:11]
	v_lshl_add_u64 v[0:1], v[0:1], 0, s[10:11]
	v_lshl_add_u64 v[2:3], v[2:3], 0, s[10:11]
	global_load_dword v9, v[0:1], off
	global_load_dword v10, v[2:3], off
	global_load_dword v11, v[0:1], off offset:2048
	global_load_dword v12, v[2:3], off offset:2048
	v_add_u32_e32 v221, 0x800, v221
	s_waitcnt vmcnt(0)
	ds_write2st64_b32 v4, v5, v6 offset1:32
	ds_write2st64_b32 v4, v7, v8 offset0:8 offset1:40
	ds_write2st64_b32 v4, v9, v10 offset0:16 offset1:48
	ds_write2st64_b32 v4, v11, v12 offset0:24 offset1:56
	s_or_b64 exec, exec, s[8:9]
